# RWKV last stage (Y and state update): operands independent of U prefetched before the preceding wave-group barrier; only the three U fragments are read after it
# baseline (speedup 1.0000x reference)
; #define LAS __attribute__((address_space(3)))
; __device__ __forceinline__ unsigned long long pack4bf(f32x4 v) { return (unsigned long long)pk2(v[0], v[1]) | ((unsigned long long)pk2(v[2], v[3]) << 32); }
; __device__ __forceinline__ void rwkv_chunk_unit(Frame& F, int unit, LAS unsigned char* regB, LAS unsigned* bcnt, unsigned& btarget) {
;     ...
;         { yv = __builtin_amdgcn_mfma_f32_16x16x32_bf16(*(const LAS s16x8*)(G3b + (16 * mi + fr) * LS + 8 * fq), *(const LAS s16x8*)(Ubt + (16 * nj + fr) * LS + 8 * fq), yv, 0, 0, 0);
;           float* yp = YRAW + ((size_t)b * SEQ + ch * 32 + 16 * mi + 4 * fq) * RD + h * 64 + half * 32 + 16 * nj + fr;
; #pragma unroll
;           for (int rg_ = 0; rg_ < 4; ++rg_) yp[(size_t)rg_ * RD] = yv[rg_]; }
;         { const int kt = w; const s16x8 bt_ = tr_frag(Bt, KS, 8 * fq, 16 * kt, fr), kt_ = tr_frag(Kt, KS, 8 * fq, 16 * kt, fr); const f32x4 gl4 = *(const LAS f32x4*)(glf + 16 * kt + 4 * fq);
; #pragma unroll
;           for (int vt = 0; vt < 2; ++vt) {
;               st[vt] = __builtin_amdgcn_mfma_f32_16x16x32_bf16(bt_, *(const LAS s16x8*)(Ubt + (16 * vt + fr) * LS + 8 * fq), st[vt], 0, 0, 0);
;               st[vt] = __builtin_amdgcn_mfma_f32_16x16x32_bf16(kt_, tr_frag(Vv, LS, 8 * fq, 16 * vt, fr), st[vt], 0, 0, 0);
;               st[vt] = st[vt] * gl4;
;               *(LAS unsigned long long*)(Sb + (16 * vt + fr) * KS + 16 * kt + 4 * fq) = pack4bf(st[vt]); } }
.LBB0_989:
	s_waitcnt vmcnt(2)
	ds_read_b128 v[10:13], v177
	ds_read_b128 v[14:17], v190
	ds_read_b128 v[244:247], v192
	s_cmp_lg_u32 s18, 64
	s_mov_b32 s10, s18
	s_waitcnt lgkmcnt(2)
	v_mfma_f32_16x16x32_bf16 v[2:5], v[212:215], v[10:13], v[2:5]
	s_waitcnt lgkmcnt(1)
	v_mfma_f32_16x16x32_bf16 v[14:17], v[216:219], v[14:17], v[90:93]
	v_mfma_f32_16x16x32_bf16 v[14:17], v[220:223], v[228:231], v[14:17]
	s_waitcnt lgkmcnt(0)
	v_mfma_f32_16x16x32_bf16 v[6:9], v[216:219], v[244:247], v[78:81]
	v_mfma_f32_16x16x32_bf16 v[6:9], v[220:223], v[232:235], v[6:9]
	v_lshl_add_u64 v[10:11], v[160:161], 0, s[0:1]
	v_lshlrev_b64 v[10:11], 12, v[10:11]
	v_lshl_add_u64 v[10:11], v[164:165], 0, v[10:11]
	v_add_co_u32_e32 v12, vcc, 0x1000, v10
	s_nop 1
	v_addc_co_u32_e32 v13, vcc, 0, v11, vcc
	v_add_co_u32_e32 v244, vcc, 0x2000, v10
	s_nop 1
	v_addc_co_u32_e32 v245, vcc, 0, v11, vcc
	v_add_co_u32_e32 v246, vcc, 0x3000, v10
	s_nop 1
	v_addc_co_u32_e32 v247, vcc, 0, v11, vcc
	global_store_dword v[10:11], v2, off
	global_store_dword v[12:13], v3, off
	global_store_dword v[244:245], v4, off
	global_store_dword v[246:247], v5, off
	v_lshlrev_b32_e32 v18, 16, v241
	v_and_b32_e32 v19, 0xffff0000, v241
	v_pk_mul_f32 v[92:93], v[226:227], v[16:17]
	v_pk_mul_f32 v[90:91], v[224:225], v[14:15]
	v_cvt_pk_bf16_f32 v15, v92, v93
	v_cvt_pk_bf16_f32 v14, v90, v91
	ds_write_b64 v191, v[14:15] offset:20992
	v_lshlrev_b32_e32 v14, 16, v243
	v_and_b32_e32 v15, 0xffff0000, v243
	v_lshlrev_b32_e32 v16, 16, v240
	v_pk_mul_f32 v[80:81], v[226:227], v[8:9]
	v_pk_mul_f32 v[78:79], v[224:225], v[6:7]
	v_cvt_pk_bf16_f32 v3, v80, v81
	v_cvt_pk_bf16_f32 v2, v78, v79
	v_lshlrev_b32_e32 v12, 16, v242
	v_and_b32_e32 v13, 0xffff0000, v242
	v_and_b32_e32 v17, 0xffff0000, v240
	ds_write_b64 v191, v[2:3] offset:23296
	s_cbranch_scc0 .LBB0_967

; #define LAS __attribute__((address_space(3)))
; __device__ __forceinline__ unsigned long long pack4bf(f32x4 v) { return (unsigned long long)pk2(v[0], v[1]) | ((unsigned long long)pk2(v[2], v[3]) << 32); }
; __device__ __forceinline__ void rwkv_chunk_unit(Frame& F, int unit, LAS unsigned char* regB, LAS unsigned* bcnt, unsigned& btarget) {
;     ...
;         { f32x4 z = (f32x4){0.f, 0.f, 0.f, 0.f};
;           z = __builtin_amdgcn_mfma_f32_16x16x32_bf16(*(const LAS s16x8*)(Acb + 32 * LS + (16 * mi + fr) * LS + 8 * fq), *(const LAS s16x8*)(RHt + (16 * nj + fr) * LS + 8 * fq), z, 0, 0, 0);
;           *(LAS unsigned long long*)(Ubt + (16 * nj + fr) * LS + 16 * mi + 4 * fq) = pack4bf(z); }
;         rw_bar(bcnt, btarget, lane);
;     ...
;         { const int kt = w; const s16x8 bt_ = tr_frag(Bt, KS, 8 * fq, 16 * kt, fr), kt_ = tr_frag(Kt, KS, 8 * fq, 16 * kt, fr); const f32x4 gl4 = *(const LAS f32x4*)(glf + 16 * kt + 4 * fq);
; #pragma unroll
;           for (int vt = 0; vt < 2; ++vt) {
;               st[vt] = __builtin_amdgcn_mfma_f32_16x16x32_bf16(bt_, *(const LAS s16x8*)(Ubt + (16 * vt + fr) * LS + 8 * fq), st[vt], 0, 0, 0);
;               st[vt] = __builtin_amdgcn_mfma_f32_16x16x32_bf16(kt_, tr_frag(Vv, LS, 8 * fq, 16 * vt, fr), st[vt], 0, 0, 0);
.LBB0_1051:
	ds_read_b128 v[6:9], v173 offset:40960
	ds_read_b128 v[10:13], v175
	s_waitcnt lgkmcnt(0)
	v_mfma_f32_16x16x32_bf16 v[6:9], v[6:9], v[10:13], 0
	s_nop 7
	v_cvt_pk_bf16_f32 v6, v6, v7
	v_cvt_pk_bf16_f32 v7, v8, v9
	ds_write_b64 v176, v[6:7]
	ds_read_b128 v[212:215], v173 offset:28160
	ds_read_b64_tr_b16 v[216:217], v178 offset:4608
	ds_read_b64_tr_b16 v[218:219], v178 offset:5184
	ds_read_b64_tr_b16 v[220:221], v178 offset:9216
	ds_read_b64_tr_b16 v[222:223], v178 offset:9792
	ds_read_b128 v[224:227], v179
	ds_read_b64_tr_b16 v[228:229], v171 offset:18432
	ds_read_b64_tr_b16 v[230:231], v171 offset:18752
	ds_read_b64_tr_b16 v[232:233], v171 offset:18464
	ds_read_b64_tr_b16 v[234:235], v171 offset:18784
	s_and_saveexec_b64 s[4:5], s[6:7]
	s_cbranch_execz .LBB0_1054
	s_mov_b64 s[10:11], exec
	v_mbcnt_lo_u32_b32 v6, s10, 0
	v_mbcnt_hi_u32_b32 v6, s11, v6
	v_cmp_eq_u32_e32 vcc, 0, v6
	s_and_b64 s[96:97], exec, vcc
	s_mov_b64 exec, s[96:97]
	s_bcnt1_i32_b64 s10, s[10:11]
	v_mov_b32_e32 v6, s12
	v_mov_b32_e32 v7, s10
	s_waitcnt lgkmcnt(10)
	ds_add_u32 v6, v7
